# loop-edge trim: dead scalar state copies of the lean conversion path and two add-zero SALU removed
# speedup vs baseline: 1.0070x; 1.0070x over previous
; DEVI void attn_unit8(const Params& p, char* smem, int unit, int l, int& cvs  , CvRun& crun) {
;     ...
;     for (int T = 0; T + 1 < NTILE; ++T) {
;         const char* Kb = K_lds + s0 * 24576; const int vb = vb0 + s0 * 16384;
;         CvRegs cvr; cv_issue(p, l, cvs, lane, cvr, crun); cvs += (int)gridDim.x * 8;
;         qkt(pB0, pB1, Kb + 12288, qr, r32, hi, cinit);
.LBB0_666:
	s_mul_i32 s98, s89, 0x6000

; DEVI f32x4 ld_nt(const float* p) { return __builtin_nontemporal_load((const f32x4*)p); }
; DEVI CvSlice cv_slice(const Params& p, int l, int s, int lane) {
;     CvSlice c;
;     if (s < NS_W13) {
;         const int e = s >> 9, r = s & 511, hb = r & 7, mat = (r >> 3) & 1, ks = r >> 4;
;         const float* W = mat ? (e < NE ? p.w3 + ((size_t)l * NE + e) * 1024 * 256 : p.ws3 + (size_t)l * 1024 * 256)
;                              : (e < NE ? p.w1 + ((size_t)l * NE + e) * 1024 * 256 : p.ws1 + (size_t)l * 1024 * 256);
;         const int hc0 = hb * 32;
;         c.src = W + hc0 + (lane & 7) * 4; c.ld = 256; c.dst = p.w13t + (size_t)e * 512 * 1024; c.K = 1024;
;         c.r0 = (hc0 >> 7) * 256 + ((hc0 >> 5) & 3) * 32 + mat * 16; c.k0 = ks * 32; c.perm = 0;
;     } else {
;         s -= NS_W13;
;         const int e = s >> 8, r = s & 255, nb = r & 31, ks = r >> 5;
;         const float* W2 = e < NE ? p.w2 + ((size_t)l * NE + e) * 256 * 1024 : p.ws2 + (size_t)l * 256 * 1024;
;         c.src = W2 + nb * 32 + (lane & 7) * 4; c.ld = 1024; c.dst = p.w2t + (size_t)e * 1024 * 256; c.K = 256; c.r0 = (nb >> 3) * 256 + ((nb & 7) >> 1) * 32 + (nb & 1) * 8; c.k0 = ks * 32; c.perm = 1;
;     }
;     return c;
; }
; DEVI void cv_next(const Params& p, int l, int s, int lane, int stride, CvRun& run) {
;     ...
;     run.c = cv_slice(p, l, s, lane); run.left = 0;
;     if ((stride & 511) == 0) {
;         if (s < NS_W13) { const int e = s >> 9, es = stride >> 9; if (e < NE) { run.left = (NE - 1 - e) / es; run.sstep = (long)es * 1024 * 256; run.dstep = (long)es * 512 * 1024; } }
;         else { const int e = (s - NS_W13) >> 8, es = stride >> 8; if (e < NE) { run.left = (NE - 1 - e) / es; run.sstep = (long)es * 256 * 1024; run.dstep = (long)es * 1024 * 256; } } }
; }
; DEVI void cv_issue(const Params& p, int l, int s, int lane, CvRegs& R, CvRun& run) {
;     R.live = s < NS_SLICES ? 1 : 0;
;     if (R.live) { cv_next(p, l, s, lane, (int)gridDim.x * 8, run); R.c = run.c; const int kq = lane >> 3;
;         const float* sp = R.c.src + (size_t)(R.c.k0 + 2 * kq) * R.c.ld;
;         R.a0 = ld_nt(sp); R.b0 = ld_nt(sp + R.c.ld); R.a1 = ld_nt(sp + (size_t)16 * R.c.ld); R.b1 = ld_nt(sp + (size_t)17 * R.c.ld); }
	v_add_u32_e32 v86, s98, v129
	ds_read_b128 v[82:85], v86 offset:12288
	ds_read_b128 v[124:127], v86 offset:18432
	s_cmp_lt_i32 s54, 0x30300
	s_mov_b32 s61, s2
	s_cselect_b64 s[14:15], -1, 0
	s_cmp_gt_i32 s54, 0x302ff
	s_mov_b32 s2, s6
	s_cbranch_scc1 .LBB0_696
	s_cmp_lt_i32 s56, 1
	s_mov_b64 s[16:17], -1
	s_cbranch_scc0 .LBB0_693
	s_lshl_b32 s71, s54, 5
	s_lshl_b32 s84, s54, 4
	s_lshl_b32 s85, s54, 3
	s_lshl_b32 s88, s54, 1
	s_lshl_b32 s70, s54, 10
	s_add_i32 s70, s70, 0xf7f80000
	s_cmp_gt_i32 s54, 0x201ff
	s_cselect_b64 s[16:17], -1, 0
	s_mov_b64 s[6:7], -1
	s_and_b64 vcc, exec, s[16:17]
	s_cbranch_vccz .LBB0_670
	s_add_i32 s6, s54, 0xfffdfe00
	s_lshr_b32 s8, s6, 8
	s_and_b32 s10, s54, 0xe0
	s_cmp_lt_u32 s6, 0x10000
	s_cselect_b64 s[6:7], -1, 0
	s_and_b32 s11, s70, 0x3fc0000
	s_and_b64 s[6:7], s[6:7], exec
	s_cselect_b32 s6, 0xc0, s78
	s_cselect_b32 s11, s11, 0
	s_add_u32 s6, s24, s6
	s_addc_u32 s7, s25, 0
	s_load_dwordx2 s[6:7], s[6:7], 0x0
	s_lshl_b32 s11, s11, 2
	s_load_dwordx2 s[20:21], s[24:25], 0x158
	s_waitcnt lgkmcnt(0)
	s_add_u32 s6, s6, s11
	s_addc_u32 s7, s7, 0
	s_and_b32 s11, s71, 0x3e0
	s_lshl_b32 s11, s11, 2
	s_add_u32 s18, s6, s11
	s_addc_u32 s19, s7, 0
	s_lshl_b64 s[6:7], s[8:9], 19
	s_add_u32 s20, s20, s6
	s_addc_u32 s21, s21, s7
	s_and_b32 s6, s71, 0x300
	s_and_b32 s7, s84, 0x60
	s_or_b32 s6, s6, s7
	s_and_b32 s7, s85, 8
	s_or_b32 s8, s6, s7
	s_mov_b64 s[6:7], 0

; DEVI void cv_next(const Params& p, int l, int s, int lane, int stride, CvRun& run) {
.LBB0_693:
	s_and_b64 vcc, exec, s[16:17]
	s_cbranch_vccz .LBB0_695
	s_lshl_b64 s[6:7], s[26:27], 1
	s_lshl_b64 s[16:17], s[28:29], 2
	s_add_u32 s68, s68, s16
	s_addc_u32 s69, s69, s17
	s_add_u32 s40, s40, s6
	s_addc_u32 s41, s41, s7
	s_add_i32 s56, s56, -1


	s_mov_b32 s95, s55

; DEVI f32x4 ld_nt(const float* p) { return __builtin_nontemporal_load((const f32x4*)p); }
; DEVI void cv_issue(const Params& p, int l, int s, int lane, CvRegs& R, CvRun& run) {
;     R.live = s < NS_SLICES ? 1 : 0;
;     if (R.live) { cv_next(p, l, s, lane, (int)gridDim.x * 8, run); R.c = run.c; const int kq = lane >> 3;
;         const float* sp = R.c.src + (size_t)(R.c.k0 + 2 * kq) * R.c.ld;
;         R.a0 = ld_nt(sp); R.b0 = ld_nt(sp + R.c.ld); R.a1 = ld_nt(sp + (size_t)16 * R.c.ld); R.b1 = ld_nt(sp + (size_t)17 * R.c.ld); }
	global_load_dwordx4 v[154:157], v242, s[68:69] nt
	global_load_dwordx4 v[158:161], v243, s[68:69] nt
	global_load_dwordx4 v[162:165], v244, s[68:69] nt
	global_load_dwordx4 v[166:169], v245, s[68:69] nt
	s_branch .LBB0_696



; DEVI void attn_unit8(const Params& p, char* smem, int unit, int l, int& cvs  , CvRun& crun) {
;     ...
;         if (T + 2 < NTILE) B_DMA(T + 2, s2);
;         qkt(pA0, pA1, K_lds + s1 * 24576, qr, r32, hi, cinit);
.LBB0_702:
	s_mul_i32 s98, s2, 0x6000
	s_add_i32 s98, s96, s98
	s_lshl_b32 s99, s2, 14
	s_add_i32 s99, s97, s99
	s_mul_i32 s6, s61, 0x6000

; DEVI void qkt(f32x16& p0, f32x16& p1, const char* Kb, const bf16x8 (&qr)[6], int r32, int hi, const f32x16& cinit) {
; #pragma unroll
;     for (int d0 = 0; d0 < 6; ++d0) { const int cb = (d0 * 16 + hi * 8) * 2;
;         const bf16x8 k0 = *(const bf16x8*)(Kb + KSWZ(r32, cb)), k1 = *(const bf16x8*)(Kb + KSWZ(32 + r32, cb));
;         p0 = __builtin_amdgcn_mfma_f32_32x32x16_bf16(k0, qr[d0], d0 == 0 ? cinit : p0, 0, 0, 0);
;         p1 = __builtin_amdgcn_mfma_f32_32x32x16_bf16(k1, qr[d0], d0 == 0 ? cinit : p1, 0, 0, 0); }
	v_add_u32_e32 v249, s6, v129

; DEVI void qkt(f32x16& p0, f32x16& p1, const char* Kb, const bf16x8 (&qr)[6], int r32, int hi, const f32x16& cinit) {
; #pragma unroll
;     for (int d0 = 0; d0 < 6; ++d0) { const int cb = (d0 * 16 + hi * 8) * 2;
;         const bf16x8 k0 = *(const bf16x8*)(Kb + KSWZ(r32, cb)), k1 = *(const bf16x8*)(Kb + KSWZ(32 + r32, cb));
;         p0 = __builtin_amdgcn_mfma_f32_32x32x16_bf16(k0, qr[d0], d0 == 0 ? cinit : p0, 0, 0, 0);
;         p1 = __builtin_amdgcn_mfma_f32_32x32x16_bf16(k1, qr[d0], d0 == 0 ? cinit : p1, 0, 0, 0); }
	s_mov_b32 m0, s98
	s_barrier
	ds_read_b128 v[234:237], v249
	ds_read_b128 v[210:213], v249 offset:6144
	global_load_lds_dwordx4 v118, s[12:13]
	s_waitcnt lgkmcnt(1)
	v_mfma_f32_32x32x16_bf16 v[98:113], v[234:237], v[150:153], v[34:49]
	s_add_i32 m0, s98, 0x2000

; DEVI void qkt(f32x16& p0, f32x16& p1, const char* Kb, const bf16x8 (&qr)[6], int r32, int hi, const f32x16& cinit) {
; #pragma unroll
;     for (int d0 = 0; d0 < 6; ++d0) { const int cb = (d0 * 16 + hi * 8) * 2;
;         const bf16x8 k0 = *(const bf16x8*)(Kb + KSWZ(r32, cb)), k1 = *(const bf16x8*)(Kb + KSWZ(32 + r32, cb));
;         p0 = __builtin_amdgcn_mfma_f32_32x32x16_bf16(k0, qr[d0], d0 == 0 ? cinit : p0, 0, 0, 0);
;         p1 = __builtin_amdgcn_mfma_f32_32x32x16_bf16(k1, qr[d0], d0 == 0 ? cinit : p1, 0, 0, 0); }
	v_add_u32_e32 v126, s6, v184
	global_load_lds_dwordx4 v120, s[12:13]
	s_waitcnt lgkmcnt(0)
	v_mfma_f32_32x32x16_bf16 v[66:81], v[210:213], v[150:153], v[34:49]
	ds_read_b128 v[210:213], v126
	ds_read_b128 v[214:217], v126 offset:6144
	s_add_i32 m0, s98, 0x4000

; DEVI void qkt(f32x16& p0, f32x16& p1, const char* Kb, const bf16x8 (&qr)[6], int r32, int hi, const f32x16& cinit) {
; #pragma unroll
;     for (int d0 = 0; d0 < 6; ++d0) { const int cb = (d0 * 16 + hi * 8) * 2;
;         const bf16x8 k0 = *(const bf16x8*)(Kb + KSWZ(r32, cb)), k1 = *(const bf16x8*)(Kb + KSWZ(32 + r32, cb));
;         p0 = __builtin_amdgcn_mfma_f32_32x32x16_bf16(k0, qr[d0], d0 == 0 ? cinit : p0, 0, 0, 0);
;         p1 = __builtin_amdgcn_mfma_f32_32x32x16_bf16(k1, qr[d0], d0 == 0 ? cinit : p1, 0, 0, 0); }
	v_add_u32_e32 v126, s6, v185
	global_load_lds_dwordx4 v122, s[12:13]
	s_mov_b32 m0, s99
	s_waitcnt lgkmcnt(1)
	v_mfma_f32_32x32x16_bf16 v[98:113], v[210:213], v[138:141], v[98:113]


	global_load_lds_dwordx4 v116, s[44:45]
	s_add_i32 m0, s99, 0x2000


; template <int OFF> DEVI s16x4 tr_read(int vb) { s16x4 r; asm volatile("ds_read_b64_tr_b16 %0, %1 offset:%2" : "=&v"(r) : "v"(vb), "i"(OFF) : "memory"); return r; }
; DEVI void pv_both(f32x16& o0, f32x16& o1, int vb, bf16x8 pa0, bf16x8 pa1, bf16x8 pa2, bf16x8 pa3) {
;     const s16x4 a0 = tr_read<v_rd_off(0, 0, 0)>(vb), b0 = tr_read<v_rd_off(0, 0, 1)>(vb), a1 = tr_read<v_rd_off(0, 1, 0)>(vb), b1 = tr_read<v_rd_off(0, 1, 1)>(vb);
;     const s16x4 a2 = tr_read<v_rd_off(0, 2, 0)>(vb), b2 = tr_read<v_rd_off(0, 2, 1)>(vb), a3 = tr_read<v_rd_off(0, 3, 0)>(vb), b3 = tr_read<v_rd_off(0, 3, 1)>(vb);
;     const s16x4 c0 = tr_read<v_rd_off(1, 0, 0)>(vb), d0 = tr_read<v_rd_off(1, 0, 1)>(vb), c1 = tr_read<v_rd_off(1, 1, 0)>(vb), d1 = tr_read<v_rd_off(1, 1, 1)>(vb);
;     const s16x4 c2 = tr_read<v_rd_off(1, 2, 0)>(vb), d2 = tr_read<v_rd_off(1, 2, 1)>(vb), c3 = tr_read<v_rd_off(1, 3, 0)>(vb), d3 = tr_read<v_rd_off(1, 3, 1)>(vb);
; DEVI void finishSM(f32x16& p0, f32x16& p1, float alpha, float& l_reg, bf16x8& pa0, bf16x8& pa1, bf16x8& pa2, bf16x8& pa3) {
; #pragma unroll
;     for (int r = 0; r < 16; ++r) p1[r] = __builtin_amdgcn_exp2f(p1[r]);
;     f32x2 s2 = (f32x2){p0[0], p0[1]} + (f32x2){p1[0], p1[1]};
; #pragma unroll
;     for (int r = 2; r < 16; r += 2) s2 += (f32x2){p0[r], p0[r + 1]} + (f32x2){p1[r], p1[r + 1]};
;     float ps = s2[0] + s2[1];
;     { auto rr = __builtin_amdgcn_permlane32_swap(__float_as_uint(ps), __float_as_uint(ps), false, false);
;       ps = __uint_as_float(rr[0]) + __uint_as_float(rr[1]); }
;     l_reg = l_reg * alpha + ps;
;     ...
;     PK4(p0, 0, pa0); PK4(p0, 8, pa1); PK4(p1, 0, pa2); PK4(p1, 8, pa3);
;     ...
; }
; DEVI void qkt(f32x16& p0, f32x16& p1, const char* Kb, const bf16x8 (&qr)[6], int r32, int hi, const f32x16& cinit) {
; #pragma unroll
;     for (int d0 = 0; d0 < 6; ++d0) { const int cb = (d0 * 16 + hi * 8) * 2;
;         const bf16x8 k0 = *(const bf16x8*)(Kb + KSWZ(r32, cb)), k1 = *(const bf16x8*)(Kb + KSWZ(32 + r32, cb));
;         p0 = __builtin_amdgcn_mfma_f32_32x32x16_bf16(k0, qr[d0], d0 == 0 ? cinit : p0, 0, 0, 0);
;         p1 = __builtin_amdgcn_mfma_f32_32x32x16_bf16(k1, qr[d0], d0 == 0 ? cinit : p1, 0, 0, 0); }
; }
	s_waitcnt lgkmcnt(0)
	v_mfma_f32_32x32x16_bf16 v[66:81], v[214:217], v[138:141], v[66:81]
	global_load_lds_dwordx4 v117, s[44:45]
	ds_read_b128 v[210:213], v126
	ds_read_b128 v[214:217], v126 offset:6144
	v_add_u32_e32 v126, s6, v204
	s_waitcnt lgkmcnt(1)
	v_mfma_f32_32x32x16_bf16 v[98:113], v[210:213], v[134:137], v[98:113]
	ds_read_b128 v[210:213], v126
	ds_read_b128 v[218:221], v126 offset:6144
	v_add_u32_e32 v126, s6, v205
	s_waitcnt lgkmcnt(2)
	v_mfma_f32_32x32x16_bf16 v[66:81], v[214:217], v[134:137], v[66:81]
	ds_read_b128 v[214:217], v126
	ds_read_b128 v[222:225], v126 offset:6144
	v_add_u32_e32 v126, s6, v206
	ds_read_b128 v[226:229], v126
	ds_read_b128 v[230:233], v126 offset:6144
	v_add_f32_e32 v126, v50, v82
	v_add_f32_e32 v127, v51, v83
	v_cvt_pk_bf16_f32 v50, v50, v51
	v_cvt_pk_bf16_f32 v51, v52, v53
	s_waitcnt lgkmcnt(5)
	v_mfma_f32_32x32x16_bf16 v[98:113], v[210:213], v[130:133], v[98:113]
	v_add_f32_e64 v210, v52, v84
	v_add_f32_e64 v211, v53, v85
	v_cvt_pk_bf16_f32 v52, v54, v55
	v_cvt_pk_bf16_f32 v53, v56, v57
	v_add_f32_e64 v126, v210, v126
	v_add_f32_e64 v127, v211, v127
	v_add_f32_e64 v210, v54, v86
	v_add_f32_e64 v211, v55, v87
	v_cvt_pk_bf16_f32 v54, v58, v59
	s_waitcnt lgkmcnt(4)
	v_mfma_f32_32x32x16_bf16 v[66:81], v[218:221], v[130:133], v[66:81]
	v_add_f32_e64 v126, v210, v126
	v_add_f32_e64 v127, v211, v127
	v_add_f32_e64 v210, v56, v88
	v_add_f32_e64 v211, v57, v89
	v_cvt_pk_bf16_f32 v55, v60, v61
	v_cvt_pk_bf16_f32 v56, v62, v63
	v_cvt_pk_bf16_f32 v57, v64, v65
	v_add_f32_e64 v126, v210, v126
	v_add_f32_e64 v127, v211, v127
	v_add_f32_e32 v210, v58, v90
	v_add_f32_e32 v211, v59, v91
	v_cvt_pk_bf16_f32 v58, v82, v83
	v_cvt_pk_bf16_f32 v59, v84, v85
	s_waitcnt lgkmcnt(3)
	v_mfma_f32_32x32x16_bf16 v[98:113], v[214:217], v[146:149], v[98:113]
	v_add_f32_e64 v126, v210, v126
	v_add_f32_e64 v127, v211, v127
	v_add_f32_e64 v210, v60, v92
	v_add_f32_e64 v211, v61, v93
	v_cvt_pk_bf16_f32 v60, v86, v87
	v_cvt_pk_bf16_f32 v61, v88, v89
	v_add_f32_e64 v126, v210, v126
	v_add_f32_e64 v127, v211, v127
	v_add_f32_e32 v210, v62, v94
	v_add_f32_e32 v211, v63, v95
	v_cvt_pk_bf16_f32 v62, v90, v91
	v_cvt_pk_bf16_f32 v63, v92, v93
	s_waitcnt lgkmcnt(2)
	v_mfma_f32_32x32x16_bf16 v[66:81], v[222:225], v[146:149], v[66:81]
	v_add_f32_e64 v126, v210, v126
	v_add_f32_e64 v127, v211, v127
	v_add_f32_e64 v210, v64, v96
	v_add_f32_e64 v211, v65, v97
	v_cvt_pk_bf16_f32 v64, v94, v95
	v_cvt_pk_bf16_f32 v65, v96, v97
	ds_read_b64_tr_b16 v[154:155], v202 offset:0x2000
	ds_read_b64_tr_b16 v[156:157], v202 offset:0x2400
	ds_read_b64_tr_b16 v[158:159], v202 offset:0x2800
	ds_read_b64_tr_b16 v[160:161], v202 offset:0x2c00
	ds_read_b64_tr_b16 v[162:163], v202 offset:0x3000
	ds_read_b64_tr_b16 v[164:165], v202 offset:0x3400
	ds_read_b64_tr_b16 v[166:167], v202 offset:0x3800
	ds_read_b64_tr_b16 v[168:169], v202 offset:0x3c00
	v_add_f32_e64 v126, v210, v126
	v_add_f32_e64 v127, v211, v127
	ds_read_b64_tr_b16 v[210:211], v202 offset:0x2200
	ds_read_b64_tr_b16 v[212:213], v202 offset:0x2600
	ds_read_b64_tr_b16 v[214:215], v202 offset:0x2a00
	s_waitcnt lgkmcnt(12)
	v_mfma_f32_32x32x16_bf16 v[98:113], v[226:229], v[142:145], v[98:113]
	ds_read_b64_tr_b16 v[216:217], v202 offset:0x2e00
	ds_read_b64_tr_b16 v[218:219], v202 offset:0x3200
	ds_read_b64_tr_b16 v[220:221], v202 offset:0x3600
	ds_read_b64_tr_b16 v[222:223], v202 offset:0x3a00
	ds_read_b64_tr_b16 v[224:225], v202 offset:0x3e00
	v_add_f32_e32 v126, v126, v127
	s_waitcnt lgkmcnt(15)
	v_mfma_f32_32x32x16_bf16 v[66:81], v[230:233], v[142:145], v[66:81]
	v_mov_b32_e32 v127, v126


; #define SBAR() __builtin_amdgcn_sched_barrier(0)
; DEVI void pv_both(f32x16& o0, f32x16& o1, int vb, bf16x8 pa0, bf16x8 pa1, bf16x8 pa2, bf16x8 pa3) {
;     ...
;     asm volatile("s_waitcnt lgkmcnt(8)" ::: "memory"); SBAR();
;     ...
;     o0 = __builtin_amdgcn_mfma_f32_32x32x16_bf16(pa0, PK(a0, b0), o0, 0, 0, 0);
;     o0 = __builtin_amdgcn_mfma_f32_32x32x16_bf16(pa1, PK(a1, b1), o0, 0, 0, 0);
;     o0 = __builtin_amdgcn_mfma_f32_32x32x16_bf16(pa2, PK(a2, b2), o0, 0, 0, 0);
;     o0 = __builtin_amdgcn_mfma_f32_32x32x16_bf16(pa3, PK(a3, b3), o0, 0, 0, 0);
;     asm volatile("s_waitcnt lgkmcnt(0)" ::: "memory"); SBAR();
;     o1 = __builtin_amdgcn_mfma_f32_32x32x16_bf16(pa0, PK(c0, d0), o1, 0, 0, 0);
;     o1 = __builtin_amdgcn_mfma_f32_32x32x16_bf16(pa1, PK(c1, d1), o1, 0, 0, 0);
;     o1 = __builtin_amdgcn_mfma_f32_32x32x16_bf16(pa2, PK(c2, d2), o1, 0, 0, 0);
;     o1 = __builtin_amdgcn_mfma_f32_32x32x16_bf16(pa3, PK(c3, d3), o1, 0, 0, 0);
;     ...
; }
; template <bool FIRST> DEVI bool partialSM(f32x16& p0, f32x16& p1, float& m_reg, float& alpha) {
;     float pmax = p0[0];
; #pragma unroll
;     for (int r = 1; r < 16; ++r) pmax = fmaxf(pmax, p0[r]);
; #pragma unroll
;     for (int r = 0; r < 16; ++r) pmax = fmaxf(pmax, p1[r]);
;     { auto rr = __builtin_amdgcn_permlane32_swap(__float_as_uint(pmax), __float_as_uint(pmax), false, false);
;       pmax = fmaxf(__uint_as_float(rr[0]), __uint_as_float(rr[1])); }
;     if (FIRST) { m_reg = pmax; alpha = 1.f;
; #pragma unroll
;         for (int r = 0; r < 16; ++r) { p0[r] = __builtin_amdgcn_exp2f(p0[r] - pmax); p1[r] = p1[r] - pmax; }
;         return false;
;     } else if (__builtin_expect(__all(pmax <= ATT_THR), 1)) { alpha = 1.f;
; #pragma unroll
;         for (int r = 0; r < 16; ++r) p0[r] = __builtin_amdgcn_exp2f(p0[r]);
	s_waitcnt lgkmcnt(14)
	v_mfma_f32_32x32x16_bf16 v[18:33], v[50:53], v[154:157], v[18:33]
	v_permlane32_swap_b32_e32 v126, v127
	s_waitcnt lgkmcnt(6)
	v_mfma_f32_32x32x16_bf16 v[2:17], v[50:53], v[210:213], v[2:17]
	s_nop 1
	v_max_f32_e32 v249, v99, v99
	v_max_f32_e32 v250, v98, v98
	v_max_f32_e32 v249, v250, v249
	v_max3_f32 v249, v249, v100, v101
	v_max3_f32 v249, v249, v102, v103
	v_max3_f32 v251, v249, v104, v105
	v_max3_f32 v251, v251, v106, v107
	v_exp_f32_e32 v50, v98
	v_exp_f32_e32 v51, v99
	v_exp_f32_e32 v52, v100
	v_exp_f32_e32 v53, v101
	v_mfma_f32_32x32x16_bf16 v[18:33], v[54:57], v[158:161], v[18:33]
	s_waitcnt lgkmcnt(4)
	v_mfma_f32_32x32x16_bf16 v[2:17], v[54:57], v[214:217], v[2:17]
	v_max3_f32 v251, v251, v108, v109
	v_max3_f32 v251, v251, v110, v111
	v_max3_f32 v251, v251, v112, v113
	v_max3_f32 v251, v251, v66, v67
	v_max3_f32 v251, v251, v68, v69
	v_max3_f32 v251, v251, v70, v71
	v_max3_f32 v251, v251, v72, v73
	v_exp_f32_e32 v54, v102
	v_exp_f32_e32 v55, v103
	v_exp_f32_e32 v56, v104
	v_exp_f32_e32 v57, v105
	v_mfma_f32_32x32x16_bf16 v[18:33], v[58:61], v[162:165], v[18:33]
	s_waitcnt lgkmcnt(2)
	v_mfma_f32_32x32x16_bf16 v[2:17], v[58:61], v[218:221], v[2:17]
	v_max3_f32 v251, v251, v74, v75
	v_max3_f32 v251, v251, v76, v77
	v_max3_f32 v251, v251, v78, v79
	v_max3_f32 v251, v251, v80, v81
	v_mov_b32_e32 v252, v251


; #define SBAR() __builtin_amdgcn_sched_barrier(0)
; DEVI void pv_both(f32x16& o0, f32x16& o1, int vb, bf16x8 pa0, bf16x8 pa1, bf16x8 pa2, bf16x8 pa3) {
;     ...
;     asm volatile("s_waitcnt lgkmcnt(0)" ::: "memory"); SBAR();
;     o1 = __builtin_amdgcn_mfma_f32_32x32x16_bf16(pa0, PK(c0, d0), o1, 0, 0, 0);
;     o1 = __builtin_amdgcn_mfma_f32_32x32x16_bf16(pa1, PK(c1, d1), o1, 0, 0, 0);
;     o1 = __builtin_amdgcn_mfma_f32_32x32x16_bf16(pa2, PK(c2, d2), o1, 0, 0, 0);
;     o1 = __builtin_amdgcn_mfma_f32_32x32x16_bf16(pa3, PK(c3, d3), o1, 0, 0, 0);
;     ...
; }
; template <bool FIRST> DEVI bool partialSM(f32x16& p0, f32x16& p1, float& m_reg, float& alpha) {
;     float pmax = p0[0];
; #pragma unroll
;     for (int r = 1; r < 16; ++r) pmax = fmaxf(pmax, p0[r]);
; #pragma unroll
;     for (int r = 0; r < 16; ++r) pmax = fmaxf(pmax, p1[r]);
;     { auto rr = __builtin_amdgcn_permlane32_swap(__float_as_uint(pmax), __float_as_uint(pmax), false, false);
;       pmax = fmaxf(__uint_as_float(rr[0]), __uint_as_float(rr[1])); }
;     if (FIRST) { m_reg = pmax; alpha = 1.f;
; #pragma unroll
;         for (int r = 0; r < 16; ++r) { p0[r] = __builtin_amdgcn_exp2f(p0[r] - pmax); p1[r] = p1[r] - pmax; }
;         return false;
;     } else if (__builtin_expect(__all(pmax <= ATT_THR), 1)) { alpha = 1.f;
; #pragma unroll
;         for (int r = 0; r < 16; ++r) p0[r] = __builtin_amdgcn_exp2f(p0[r]);
;         return false;
;     } else { const float d = fmaxf(pmax, 0.f); alpha = __builtin_amdgcn_exp2f(-d); m_reg += d;
	v_exp_f32_e32 v58, v106
	v_exp_f32_e32 v59, v107
	v_permlane32_swap_b32_e32 v251, v252
	v_exp_f32_e32 v60, v108
	v_exp_f32_e32 v61, v109
	v_mfma_f32_32x32x16_bf16 v[18:33], v[62:65], v[166:169], v[18:33]
	s_waitcnt lgkmcnt(0)
	v_mfma_f32_32x32x16_bf16 v[2:17], v[62:65], v[222:225], v[2:17]
	v_exp_f32_e32 v62, v110
	v_exp_f32_e32 v63, v111
	v_exp_f32_e32 v64, v112
	v_exp_f32_e32 v65, v113
	v_max_f32_e32 v252, v252, v252
	v_max_f32_e32 v251, v251, v251
	v_max_f32_e32 v174, v251, v252
	v_cmp_ge_f32_e32 vcc, s79, v174
	s_cmp_lg_u64 vcc, exec
	s_cselect_b64 s[6:7], -1, 0
	s_cbranch_scc1 .LBB0_711
	v_mov_b32_e32 v202, 1.0

; template <bool FIRST> DEVI bool partialSM(f32x16& p0, f32x16& p1, float& m_reg, float& alpha) {
;     ...
;     } else if (__builtin_expect(__all(pmax <= ATT_THR), 1)) { alpha = 1.f;
; #pragma unroll
;         for (int r = 0; r < 16; ++r) p0[r] = __builtin_amdgcn_exp2f(p0[r]);
;         return false;
;     } else { const float d = fmaxf(pmax, 0.f); alpha = __builtin_amdgcn_exp2f(-d); m_reg += d;
; #pragma unroll
;         for (int r = 0; r < 16; ++r) { p0[r] = __builtin_amdgcn_exp2f(p0[r] - d); p1[r] = p1[r] - d; }
;         return true;
;     }
	s_branch .LBB0_716

; DEVI void attn_unit8(const Params& p, char* smem, int unit, int l, int& cvs  , CvRun& crun) {
;     ...
;     for (int T = 0; T + 1 < NTILE; ++T) {
;         const char* Kb = K_lds + s0 * 24576; const int vb = vb0 + s0 * 16384;
;         CvRegs cvr; cv_issue(p, l, cvs, lane, cvr, crun); cvs += (int)gridDim.x * 8;
;         qkt(pB0, pB1, Kb + 12288, qr, r32, hi, cinit);
.LBB0_2230:
	s_mul_i32 s98, s71, 0x6000

; DEVI CvSlice cv_slice(const Params& p, int l, int s, int lane) {
;     CvSlice c;
;     if (s < NS_W13) {
;         const int e = s >> 9, r = s & 511, hb = r & 7, mat = (r >> 3) & 1, ks = r >> 4;
;         const float* W = mat ? (e < NE ? p.w3 + ((size_t)l * NE + e) * 1024 * 256 : p.ws3 + (size_t)l * 1024 * 256)
;                              : (e < NE ? p.w1 + ((size_t)l * NE + e) * 1024 * 256 : p.ws1 + (size_t)l * 1024 * 256);
;         const int hc0 = hb * 32;
;         c.src = W + hc0 + (lane & 7) * 4; c.ld = 256; c.dst = p.w13t + (size_t)e * 512 * 1024; c.K = 1024;
;         c.r0 = (hc0 >> 7) * 256 + ((hc0 >> 5) & 3) * 32 + mat * 16; c.k0 = ks * 32; c.perm = 0;
;     } else {
;         s -= NS_W13;
;         const int e = s >> 8, r = s & 255, nb = r & 31, ks = r >> 5;
;         const float* W2 = e < NE ? p.w2 + ((size_t)l * NE + e) * 256 * 1024 : p.ws2 + (size_t)l * 256 * 1024;
;         c.src = W2 + nb * 32 + (lane & 7) * 4; c.ld = 1024; c.dst = p.w2t + (size_t)e * 1024 * 256; c.K = 256; c.r0 = (nb >> 3) * 256 + ((nb & 7) >> 1) * 32 + (nb & 1) * 8; c.k0 = ks * 32; c.perm = 1;
;     }
;     return c;
; }
; DEVI void cv_next(const Params& p, int l, int s, int lane, int stride, CvRun& run) {
;     ...
;     run.c = cv_slice(p, l, s, lane); run.left = 0;
;     if ((stride & 511) == 0) {
;         if (s < NS_W13) { const int e = s >> 9, es = stride >> 9; if (e < NE) { run.left = (NE - 1 - e) / es; run.sstep = (long)es * 1024 * 256; run.dstep = (long)es * 512 * 1024; } }
;         else { const int e = (s - NS_W13) >> 8, es = stride >> 8; if (e < NE) { run.left = (NE - 1 - e) / es; run.sstep = (long)es * 256 * 1024; run.dstep = (long)es * 1024 * 256; } } }
; }
; DEVI void cv_issue(const Params& p, int l, int s, int lane, CvRegs& R, CvRun& run) {
;     R.live = s < NS_SLICES ? 1 : 0;
;     if (R.live) { cv_next(p, l, s, lane, (int)gridDim.x * 8, run); R.c = run.c; const int kq = lane >> 3;
;         const float* sp = R.c.src + (size_t)(R.c.k0 + 2 * kq) * R.c.ld;
;         R.a0 = ld_nt(sp); R.b0 = ld_nt(sp + R.c.ld); R.a1 = ld_nt(sp + (size_t)16 * R.c.ld); R.b1 = ld_nt(sp + (size_t)17 * R.c.ld); }
; DEVI void attn_unit8(const Params& p, char* smem, int unit, int l, int& cvs  , CvRun& crun) {
;     ...
;         const char* Kb = K_lds + s0 * 24576; const int vb = vb0 + s0 * 16384;
;         CvRegs cvr; cv_issue(p, l, cvs, lane, cvr, crun); cvs += (int)gridDim.x * 8;
	v_add_u32_e32 v86, s98, v129
	ds_read_b128 v[82:85], v86 offset:12288
	ds_read_b128 v[124:127], v86 offset:18432
	s_cmp_lt_i32 s54, 0x30300
	s_mov_b32 s2, s61
	s_cselect_b64 s[14:15], -1, 0
	s_cmp_gt_i32 s54, 0x302ff
	s_mov_b32 s61, s6
	s_cbranch_scc1 .LBB0_2260
	s_cmp_lt_i32 s56, 1
	s_mov_b64 s[16:17], -1
	s_cbranch_scc0 .LBB0_2257
	s_lshl_b32 s84, s54, 5
	s_lshl_b32 s85, s54, 4
	s_lshl_b32 s88, s54, 3
	s_lshl_b32 s70, s54, 1
	s_lshl_b32 s89, s54, 10
	s_add_i32 s89, s89, 0xf7f80000
	s_cmp_gt_i32 s54, 0x201ff
	s_cselect_b64 s[16:17], -1, 0
	s_mov_b64 s[6:7], -1
	s_and_b64 vcc, exec, s[16:17]
	s_cbranch_vccz .LBB0_2234
	s_add_i32 s6, s54, 0xfffdfe00
	s_lshr_b32 s8, s6, 8
	s_and_b32 s10, s54, 0xe0
	s_cmp_lt_u32 s6, 0x10000
	s_cselect_b64 s[6:7], -1, 0
	s_and_b32 s11, s89, 0x3fc0000
	s_bitset1_b32 s11, 26
	s_and_b64 s[6:7], s[6:7], exec
	s_cselect_b32 s6, 0xc0, s79
	s_cselect_b32 s11, s11, 0x40000
	s_add_u32 s6, s24, s6
	s_addc_u32 s7, s25, 0
	s_load_dwordx2 s[6:7], s[6:7], 0x0
	s_lshl_b32 s11, s11, 2
	s_load_dwordx2 s[20:21], s[24:25], 0x158
	s_waitcnt lgkmcnt(0)
	s_add_u32 s6, s6, s11
	s_addc_u32 s7, s7, 0
	s_and_b32 s11, s84, 0x3e0
	s_lshl_b32 s11, s11, 2
	s_add_u32 s18, s6, s11
	s_addc_u32 s19, s7, 0
	s_lshl_b64 s[6:7], s[8:9], 19
	s_add_u32 s20, s20, s6
	s_addc_u32 s21, s21, s7
	s_and_b32 s6, s84, 0x300
	s_and_b32 s7, s85, 0x60
	s_or_b32 s6, s6, s7
	s_and_b32 s7, s88, 8
	s_or_b32 s8, s6, s7
	s_mov_b64 s[6:7], 0

; DEVI void attn_unit8(const Params& p, char* smem, int unit, int l, int& cvs  , CvRun& crun) {
;     ...
;         if (T + 2 < NTILE) B_DMA(T + 2, s2);
;         qkt(pA0, pA1, K_lds + s1 * 24576, qr, r32, hi, cinit);
.LBB0_2266:
	s_mul_i32 s98, s61, 0x6000
	s_add_i32 s98, s96, s98
	s_lshl_b32 s99, s61, 14
	s_add_i32 s99, s97, s99
	s_mul_i32 s6, s2, 0x6000

; DEVI void qkt(f32x16& p0, f32x16& p1, const char* Kb, const bf16x8 (&qr)[6], int r32, int hi, const f32x16& cinit) {
; #pragma unroll
;     for (int d0 = 0; d0 < 6; ++d0) { const int cb = (d0 * 16 + hi * 8) * 2;
;         const bf16x8 k0 = *(const bf16x8*)(Kb + KSWZ(r32, cb)), k1 = *(const bf16x8*)(Kb + KSWZ(32 + r32, cb));
;         p0 = __builtin_amdgcn_mfma_f32_32x32x16_bf16(k0, qr[d0], d0 == 0 ? cinit : p0, 0, 0, 0);
;         p1 = __builtin_amdgcn_mfma_f32_32x32x16_bf16(k1, qr[d0], d0 == 0 ? cinit : p1, 0, 0, 0); }
	v_add_u32_e32 v249, s6, v129

; DEVI void qkt(f32x16& p0, f32x16& p1, const char* Kb, const bf16x8 (&qr)[6], int r32, int hi, const f32x16& cinit) {
; #pragma unroll
;     for (int d0 = 0; d0 < 6; ++d0) { const int cb = (d0 * 16 + hi * 8) * 2;
;         const bf16x8 k0 = *(const bf16x8*)(Kb + KSWZ(r32, cb)), k1 = *(const bf16x8*)(Kb + KSWZ(32 + r32, cb));
;         p0 = __builtin_amdgcn_mfma_f32_32x32x16_bf16(k0, qr[d0], d0 == 0 ? cinit : p0, 0, 0, 0);
;         p1 = __builtin_amdgcn_mfma_f32_32x32x16_bf16(k1, qr[d0], d0 == 0 ? cinit : p1, 0, 0, 0); }
	s_mov_b32 m0, s98
	s_barrier
	ds_read_b128 v[234:237], v249
	ds_read_b128 v[212:215], v249 offset:6144
	global_load_lds_dwordx4 v118, s[12:13]
	s_waitcnt lgkmcnt(1)
	v_mfma_f32_32x32x16_bf16 v[98:113], v[234:237], v[150:153], v[34:49]
	s_add_i32 m0, s98, 0x2000

; DEVI void qkt(f32x16& p0, f32x16& p1, const char* Kb, const bf16x8 (&qr)[6], int r32, int hi, const f32x16& cinit) {
; #pragma unroll
;     for (int d0 = 0; d0 < 6; ++d0) { const int cb = (d0 * 16 + hi * 8) * 2;
;         const bf16x8 k0 = *(const bf16x8*)(Kb + KSWZ(r32, cb)), k1 = *(const bf16x8*)(Kb + KSWZ(32 + r32, cb));
;         p0 = __builtin_amdgcn_mfma_f32_32x32x16_bf16(k0, qr[d0], d0 == 0 ? cinit : p0, 0, 0, 0);
;         p1 = __builtin_amdgcn_mfma_f32_32x32x16_bf16(k1, qr[d0], d0 == 0 ? cinit : p1, 0, 0, 0); }
	v_add_u32_e32 v126, s6, v184
	global_load_lds_dwordx4 v120, s[12:13]
	s_waitcnt lgkmcnt(0)
	v_mfma_f32_32x32x16_bf16 v[66:81], v[212:215], v[150:153], v[34:49]
	ds_read_b128 v[212:215], v126
	ds_read_b128 v[216:219], v126 offset:6144
	s_add_i32 m0, s98, 0x4000

; DEVI void qkt(f32x16& p0, f32x16& p1, const char* Kb, const bf16x8 (&qr)[6], int r32, int hi, const f32x16& cinit) {
; #pragma unroll
;     for (int d0 = 0; d0 < 6; ++d0) { const int cb = (d0 * 16 + hi * 8) * 2;
;         const bf16x8 k0 = *(const bf16x8*)(Kb + KSWZ(r32, cb)), k1 = *(const bf16x8*)(Kb + KSWZ(32 + r32, cb));
;         p0 = __builtin_amdgcn_mfma_f32_32x32x16_bf16(k0, qr[d0], d0 == 0 ? cinit : p0, 0, 0, 0);
;         p1 = __builtin_amdgcn_mfma_f32_32x32x16_bf16(k1, qr[d0], d0 == 0 ? cinit : p1, 0, 0, 0); }
	v_add_u32_e32 v126, s6, v185
	global_load_lds_dwordx4 v122, s[12:13]
	s_mov_b32 m0, s99
	s_waitcnt lgkmcnt(1)
	v_mfma_f32_32x32x16_bf16 v[98:113], v[212:215], v[138:141], v[98:113]


	global_load_lds_dwordx4 v116, s[44:45]
	s_add_i32 m0, s99, 0x2000


; template <int OFF> DEVI s16x4 tr_read(int vb) { s16x4 r; asm volatile("ds_read_b64_tr_b16 %0, %1 offset:%2" : "=&v"(r) : "v"(vb), "i"(OFF) : "memory"); return r; }
; DEVI void pv_both(f32x16& o0, f32x16& o1, int vb, bf16x8 pa0, bf16x8 pa1, bf16x8 pa2, bf16x8 pa3) {
;     const s16x4 a0 = tr_read<v_rd_off(0, 0, 0)>(vb), b0 = tr_read<v_rd_off(0, 0, 1)>(vb), a1 = tr_read<v_rd_off(0, 1, 0)>(vb), b1 = tr_read<v_rd_off(0, 1, 1)>(vb);
;     const s16x4 a2 = tr_read<v_rd_off(0, 2, 0)>(vb), b2 = tr_read<v_rd_off(0, 2, 1)>(vb), a3 = tr_read<v_rd_off(0, 3, 0)>(vb), b3 = tr_read<v_rd_off(0, 3, 1)>(vb);
;     const s16x4 c0 = tr_read<v_rd_off(1, 0, 0)>(vb), d0 = tr_read<v_rd_off(1, 0, 1)>(vb), c1 = tr_read<v_rd_off(1, 1, 0)>(vb), d1 = tr_read<v_rd_off(1, 1, 1)>(vb);
;     const s16x4 c2 = tr_read<v_rd_off(1, 2, 0)>(vb), d2 = tr_read<v_rd_off(1, 2, 1)>(vb), c3 = tr_read<v_rd_off(1, 3, 0)>(vb), d3 = tr_read<v_rd_off(1, 3, 1)>(vb);
; DEVI void finishSM(f32x16& p0, f32x16& p1, float alpha, float& l_reg, bf16x8& pa0, bf16x8& pa1, bf16x8& pa2, bf16x8& pa3) {
; #pragma unroll
;     for (int r = 0; r < 16; ++r) p1[r] = __builtin_amdgcn_exp2f(p1[r]);
;     f32x2 s2 = (f32x2){p0[0], p0[1]} + (f32x2){p1[0], p1[1]};
; #pragma unroll
;     for (int r = 2; r < 16; r += 2) s2 += (f32x2){p0[r], p0[r + 1]} + (f32x2){p1[r], p1[r + 1]};
;     float ps = s2[0] + s2[1];
;     { auto rr = __builtin_amdgcn_permlane32_swap(__float_as_uint(ps), __float_as_uint(ps), false, false);
;       ps = __uint_as_float(rr[0]) + __uint_as_float(rr[1]); }
;     l_reg = l_reg * alpha + ps;
;     ...
;     PK4(p0, 0, pa0); PK4(p0, 8, pa1); PK4(p1, 0, pa2); PK4(p1, 8, pa3);
;     ...
; }
; DEVI void qkt(f32x16& p0, f32x16& p1, const char* Kb, const bf16x8 (&qr)[6], int r32, int hi, const f32x16& cinit) {
; #pragma unroll
;     for (int d0 = 0; d0 < 6; ++d0) { const int cb = (d0 * 16 + hi * 8) * 2;
;         const bf16x8 k0 = *(const bf16x8*)(Kb + KSWZ(r32, cb)), k1 = *(const bf16x8*)(Kb + KSWZ(32 + r32, cb));
;         p0 = __builtin_amdgcn_mfma_f32_32x32x16_bf16(k0, qr[d0], d0 == 0 ? cinit : p0, 0, 0, 0);
;         p1 = __builtin_amdgcn_mfma_f32_32x32x16_bf16(k1, qr[d0], d0 == 0 ? cinit : p1, 0, 0, 0); }
; }
	s_waitcnt lgkmcnt(0)
	v_mfma_f32_32x32x16_bf16 v[66:81], v[216:219], v[138:141], v[66:81]
	global_load_lds_dwordx4 v117, s[44:45]
	ds_read_b128 v[212:215], v126
	ds_read_b128 v[216:219], v126 offset:6144
	v_add_u32_e32 v126, s6, v205
	s_waitcnt lgkmcnt(1)
	v_mfma_f32_32x32x16_bf16 v[98:113], v[212:215], v[134:137], v[98:113]
	ds_read_b128 v[212:215], v126
	ds_read_b128 v[220:223], v126 offset:6144
	v_add_u32_e32 v126, s6, v206
	s_waitcnt lgkmcnt(2)
	v_mfma_f32_32x32x16_bf16 v[66:81], v[216:219], v[134:137], v[66:81]
	ds_read_b128 v[216:219], v126
	ds_read_b128 v[224:227], v126 offset:6144
	v_add_u32_e32 v126, s6, v207
	ds_read_b128 v[228:231], v126
	ds_read_b128 v[232:235], v126 offset:6144
	v_add_f32_e32 v126, v50, v82
	v_add_f32_e32 v127, v51, v83
	v_cvt_pk_bf16_f32 v50, v50, v51
	v_cvt_pk_bf16_f32 v51, v52, v53
	s_waitcnt lgkmcnt(5)
	v_mfma_f32_32x32x16_bf16 v[98:113], v[212:215], v[130:133], v[98:113]
	v_add_f32_e64 v212, v52, v84
	v_add_f32_e64 v213, v53, v85
	v_cvt_pk_bf16_f32 v52, v54, v55
	v_cvt_pk_bf16_f32 v53, v56, v57
	v_add_f32_e64 v126, v212, v126
	v_add_f32_e64 v127, v213, v127
	v_add_f32_e64 v212, v54, v86
	v_add_f32_e64 v213, v55, v87
	v_cvt_pk_bf16_f32 v54, v58, v59
	s_waitcnt lgkmcnt(4)
	v_mfma_f32_32x32x16_bf16 v[66:81], v[220:223], v[130:133], v[66:81]
	v_add_f32_e64 v126, v212, v126
	v_add_f32_e64 v127, v213, v127
	v_add_f32_e64 v212, v56, v88
	v_add_f32_e64 v213, v57, v89
	v_cvt_pk_bf16_f32 v55, v60, v61
	v_cvt_pk_bf16_f32 v56, v62, v63
	v_cvt_pk_bf16_f32 v57, v64, v65
	v_add_f32_e64 v126, v212, v126
	v_add_f32_e64 v127, v213, v127
	v_add_f32_e32 v212, v58, v90
	v_add_f32_e32 v213, v59, v91
	v_cvt_pk_bf16_f32 v58, v82, v83
	v_cvt_pk_bf16_f32 v59, v84, v85
	s_waitcnt lgkmcnt(3)
	v_mfma_f32_32x32x16_bf16 v[98:113], v[216:219], v[146:149], v[98:113]
	v_add_f32_e64 v126, v212, v126
	v_add_f32_e64 v127, v213, v127
	v_add_f32_e64 v212, v60, v92
	v_add_f32_e64 v213, v61, v93
	v_cvt_pk_bf16_f32 v60, v86, v87
	v_cvt_pk_bf16_f32 v61, v88, v89
	v_add_f32_e64 v126, v212, v126
	v_add_f32_e64 v127, v213, v127
	v_add_f32_e32 v212, v62, v94
	v_add_f32_e32 v213, v63, v95
	v_cvt_pk_bf16_f32 v62, v90, v91
	v_cvt_pk_bf16_f32 v63, v92, v93
	s_waitcnt lgkmcnt(2)
	v_mfma_f32_32x32x16_bf16 v[66:81], v[224:227], v[146:149], v[66:81]
	v_add_f32_e64 v126, v212, v126
	v_add_f32_e64 v127, v213, v127
	v_add_f32_e64 v212, v64, v96
	v_add_f32_e64 v213, v65, v97
	v_cvt_pk_bf16_f32 v64, v94, v95
	v_cvt_pk_bf16_f32 v65, v96, v97
	ds_read_b64_tr_b16 v[154:155], v203 offset:0x2000
	ds_read_b64_tr_b16 v[156:157], v203 offset:0x2400
	ds_read_b64_tr_b16 v[158:159], v203 offset:0x2800
	ds_read_b64_tr_b16 v[160:161], v203 offset:0x2c00
	ds_read_b64_tr_b16 v[162:163], v203 offset:0x3000
	ds_read_b64_tr_b16 v[164:165], v203 offset:0x3400
	ds_read_b64_tr_b16 v[166:167], v203 offset:0x3800
	ds_read_b64_tr_b16 v[168:169], v203 offset:0x3c00
	v_add_f32_e64 v126, v212, v126
	v_add_f32_e64 v127, v213, v127
	ds_read_b64_tr_b16 v[212:213], v203 offset:0x2200
	ds_read_b64_tr_b16 v[214:215], v203 offset:0x2600
	ds_read_b64_tr_b16 v[216:217], v203 offset:0x2a00
	s_waitcnt lgkmcnt(12)
	v_mfma_f32_32x32x16_bf16 v[98:113], v[228:231], v[142:145], v[98:113]
	ds_read_b64_tr_b16 v[218:219], v203 offset:0x2e00
	ds_read_b64_tr_b16 v[220:221], v203 offset:0x3200
	ds_read_b64_tr_b16 v[222:223], v203 offset:0x3600
	ds_read_b64_tr_b16 v[224:225], v203 offset:0x3a00
	ds_read_b64_tr_b16 v[226:227], v203 offset:0x3e00
	v_add_f32_e32 v126, v126, v127
	s_waitcnt lgkmcnt(15)
	v_mfma_f32_32x32x16_bf16 v[66:81], v[232:235], v[142:145], v[66:81]
	v_mov_b32_e32 v127, v126


; #define SBAR() __builtin_amdgcn_sched_barrier(0)
; DEVI void pv_both(f32x16& o0, f32x16& o1, int vb, bf16x8 pa0, bf16x8 pa1, bf16x8 pa2, bf16x8 pa3) {
;     ...
;     asm volatile("s_waitcnt lgkmcnt(8)" ::: "memory"); SBAR();
;     ...
;     o0 = __builtin_amdgcn_mfma_f32_32x32x16_bf16(pa0, PK(a0, b0), o0, 0, 0, 0);
;     o0 = __builtin_amdgcn_mfma_f32_32x32x16_bf16(pa1, PK(a1, b1), o0, 0, 0, 0);
;     o0 = __builtin_amdgcn_mfma_f32_32x32x16_bf16(pa2, PK(a2, b2), o0, 0, 0, 0);
;     o0 = __builtin_amdgcn_mfma_f32_32x32x16_bf16(pa3, PK(a3, b3), o0, 0, 0, 0);
;     asm volatile("s_waitcnt lgkmcnt(0)" ::: "memory"); SBAR();
;     o1 = __builtin_amdgcn_mfma_f32_32x32x16_bf16(pa0, PK(c0, d0), o1, 0, 0, 0);
;     o1 = __builtin_amdgcn_mfma_f32_32x32x16_bf16(pa1, PK(c1, d1), o1, 0, 0, 0);
;     o1 = __builtin_amdgcn_mfma_f32_32x32x16_bf16(pa2, PK(c2, d2), o1, 0, 0, 0);
;     o1 = __builtin_amdgcn_mfma_f32_32x32x16_bf16(pa3, PK(c3, d3), o1, 0, 0, 0);
;     ...
; }
; template <bool FIRST> DEVI bool partialSM(f32x16& p0, f32x16& p1, float& m_reg, float& alpha) {
;     float pmax = p0[0];
; #pragma unroll
;     for (int r = 1; r < 16; ++r) pmax = fmaxf(pmax, p0[r]);
; #pragma unroll
;     for (int r = 0; r < 16; ++r) pmax = fmaxf(pmax, p1[r]);
;     { auto rr = __builtin_amdgcn_permlane32_swap(__float_as_uint(pmax), __float_as_uint(pmax), false, false);
;       pmax = fmaxf(__uint_as_float(rr[0]), __uint_as_float(rr[1])); }
;     if (FIRST) { m_reg = pmax; alpha = 1.f;
; #pragma unroll
;         for (int r = 0; r < 16; ++r) { p0[r] = __builtin_amdgcn_exp2f(p0[r] - pmax); p1[r] = p1[r] - pmax; }
;         return false;
;     } else if (__builtin_expect(__all(pmax <= ATT_THR), 1)) { alpha = 1.f;
; #pragma unroll
;         for (int r = 0; r < 16; ++r) p0[r] = __builtin_amdgcn_exp2f(p0[r]);
	s_waitcnt lgkmcnt(14)
	v_mfma_f32_32x32x16_bf16 v[18:33], v[50:53], v[154:157], v[18:33]
	v_permlane32_swap_b32_e32 v126, v127
	s_waitcnt lgkmcnt(6)
	v_mfma_f32_32x32x16_bf16 v[2:17], v[50:53], v[212:215], v[2:17]
	s_nop 1
	v_max_f32_e32 v249, v99, v99
	v_max_f32_e32 v250, v98, v98
	v_max_f32_e32 v249, v250, v249
	v_max3_f32 v249, v249, v100, v101
	v_max3_f32 v249, v249, v102, v103
	v_max3_f32 v251, v249, v104, v105
	v_max3_f32 v251, v251, v106, v107
	v_exp_f32_e32 v50, v98
	v_exp_f32_e32 v51, v99
	v_exp_f32_e32 v52, v100
	v_exp_f32_e32 v53, v101
	v_mfma_f32_32x32x16_bf16 v[18:33], v[54:57], v[158:161], v[18:33]
	s_waitcnt lgkmcnt(4)
	v_mfma_f32_32x32x16_bf16 v[2:17], v[54:57], v[216:219], v[2:17]
	v_max3_f32 v251, v251, v108, v109
	v_max3_f32 v251, v251, v110, v111
	v_max3_f32 v251, v251, v112, v113
	v_max3_f32 v251, v251, v66, v67
	v_max3_f32 v251, v251, v68, v69
	v_max3_f32 v251, v251, v70, v71
	v_max3_f32 v251, v251, v72, v73
	v_exp_f32_e32 v54, v102
	v_exp_f32_e32 v55, v103
	v_exp_f32_e32 v56, v104
	v_exp_f32_e32 v57, v105
	v_mfma_f32_32x32x16_bf16 v[18:33], v[58:61], v[162:165], v[18:33]
	s_waitcnt lgkmcnt(2)
	v_mfma_f32_32x32x16_bf16 v[2:17], v[58:61], v[220:223], v[2:17]
	v_max3_f32 v251, v251, v74, v75
	v_max3_f32 v251, v251, v76, v77
	v_max3_f32 v251, v251, v78, v79
	v_max3_f32 v251, v251, v80, v81
	v_mov_b32_e32 v252, v251


; #define SBAR() __builtin_amdgcn_sched_barrier(0)
; DEVI void pv_both(f32x16& o0, f32x16& o1, int vb, bf16x8 pa0, bf16x8 pa1, bf16x8 pa2, bf16x8 pa3) {
;     ...
;     asm volatile("s_waitcnt lgkmcnt(0)" ::: "memory"); SBAR();
;     o1 = __builtin_amdgcn_mfma_f32_32x32x16_bf16(pa0, PK(c0, d0), o1, 0, 0, 0);
;     o1 = __builtin_amdgcn_mfma_f32_32x32x16_bf16(pa1, PK(c1, d1), o1, 0, 0, 0);
;     o1 = __builtin_amdgcn_mfma_f32_32x32x16_bf16(pa2, PK(c2, d2), o1, 0, 0, 0);
;     o1 = __builtin_amdgcn_mfma_f32_32x32x16_bf16(pa3, PK(c3, d3), o1, 0, 0, 0);
;     ...
; }
; template <bool FIRST> DEVI bool partialSM(f32x16& p0, f32x16& p1, float& m_reg, float& alpha) {
;     float pmax = p0[0];
; #pragma unroll
;     for (int r = 1; r < 16; ++r) pmax = fmaxf(pmax, p0[r]);
; #pragma unroll
;     for (int r = 0; r < 16; ++r) pmax = fmaxf(pmax, p1[r]);
;     { auto rr = __builtin_amdgcn_permlane32_swap(__float_as_uint(pmax), __float_as_uint(pmax), false, false);
;       pmax = fmaxf(__uint_as_float(rr[0]), __uint_as_float(rr[1])); }
;     if (FIRST) { m_reg = pmax; alpha = 1.f;
; #pragma unroll
;         for (int r = 0; r < 16; ++r) { p0[r] = __builtin_amdgcn_exp2f(p0[r] - pmax); p1[r] = p1[r] - pmax; }
;         return false;
;     } else if (__builtin_expect(__all(pmax <= ATT_THR), 1)) { alpha = 1.f;
; #pragma unroll
;         for (int r = 0; r < 16; ++r) p0[r] = __builtin_amdgcn_exp2f(p0[r]);
;         return false;
;     } else { const float d = fmaxf(pmax, 0.f); alpha = __builtin_amdgcn_exp2f(-d); m_reg += d;
	v_exp_f32_e32 v58, v106
	v_exp_f32_e32 v59, v107
	v_permlane32_swap_b32_e32 v251, v252
	v_exp_f32_e32 v60, v108
	v_exp_f32_e32 v61, v109
	v_mfma_f32_32x32x16_bf16 v[18:33], v[62:65], v[166:169], v[18:33]
	s_waitcnt lgkmcnt(0)
	v_mfma_f32_32x32x16_bf16 v[2:17], v[62:65], v[224:227], v[2:17]
	v_exp_f32_e32 v62, v110
	v_exp_f32_e32 v63, v111
	v_exp_f32_e32 v64, v112
	v_exp_f32_e32 v65, v113
	v_max_f32_e32 v252, v252, v252
	v_max_f32_e32 v251, v251, v251
	v_max_f32_e32 v174, v251, v252
	v_cmp_ge_f32_e32 vcc, s80, v174
	s_cmp_lg_u64 vcc, exec
	s_cselect_b64 s[6:7], -1, 0
	s_cbranch_scc1 .LBB0_2275
	v_mov_b32_e32 v203, 1.0

; template <bool FIRST> DEVI bool partialSM(f32x16& p0, f32x16& p1, float& m_reg, float& alpha) {
;     ...
;     } else if (__builtin_expect(__all(pmax <= ATT_THR), 1)) { alpha = 1.f;
; #pragma unroll
;         for (int r = 0; r < 16; ++r) p0[r] = __builtin_amdgcn_exp2f(p0[r]);
;         return false;
;     } else { const float d = fmaxf(pmax, 0.f); alpha = __builtin_amdgcn_exp2f(-d); m_reg += d;
; #pragma unroll
;         for (int r = 0; r < 16; ++r) { p0[r] = __builtin_amdgcn_exp2f(p0[r] - d); p1[r] = p1[r] - d; }
;         return true;
;     }
	s_branch .LBB0_2280
